# LoRA GEMM skips the K-steps whose weight blocks are structurally zero (1 trip for decay/a tiles, 2 for gate tiles), on top of v21
# baseline (speedup 1.0000x reference)
.LBB0_1142:
	s_mov_b64 s[0:1], s[54:55]
	s_load_dword s0, s[0:1], 0x138
	s_waitcnt lgkmcnt(0)
	s_cmp_gt_i32 s0, 5
	s_cbranch_scc1 .LBB0_1158
	s_mov_b64 s[0:1], s[54:55]
	s_load_dword s0, s[0:1], 0x13c
	s_waitcnt lgkmcnt(0)
	s_cmp_lt_i32 s0, 6
	s_cbranch_scc1 .LBB0_1158
	s_mov_b64 s[0:1], s[54:55]
	v_mov_b32_e32 v1, v0
	s_waitcnt vmcnt(0)
	v_mov_b32_e32 v2, v0
	s_movk_i32 s10, 0x180
	v_readfirstlane_b32 s12, v2
	s_movk_i32 s2, 0x180
	s_andn2_b64 vcc, exec, s[8:9]
	s_cbranch_vccnz .LBB0_1158
	v_bfe_i32 v4, v2, 27, 1
	v_lshlrev_b32_e32 v3, 4, v2
	v_lshrrev_b32_e32 v4, 22, v4
	v_add_u32_e32 v4, v3, v4
	v_and_b32_e32 v4, 0xfffffc00, v4
	v_sub_u32_e32 v4, v3, v4
	v_lshrrev_b32_e32 v5, 4, v4
	v_ashrrev_i32_e32 v1, 31, v2
	v_bitop3_b32 v4, v5, v4, 32 bitop3:0x6c
	v_lshrrev_b32_e32 v1, 26, v1
	v_ashrrev_i32_e32 v6, 31, v4
	v_add_u32_e32 v1, v2, v1
	v_lshrrev_b32_e32 v6, 26, v6
	v_ashrrev_i32_e32 v1, 6, v1
	v_add_u32_e32 v6, v4, v6
	v_lshlrev_b32_e32 v5, 3, v1
	v_ashrrev_i32_e32 v7, 6, v6
	v_and_b32_e32 v6, 0xc0, v6
	v_and_b32_e32 v5, -16, v5
	v_lshlrev_b32_e32 v1, 5, v1
	v_sub_u32_e32 v4, v4, v6
	v_mov_b32_e32 v6, 1
	v_add_u32_e32 v5, v7, v5
	v_and_b32_e32 v1, 32, v1
	v_ashrrev_i16_sdwa v4, v6, sext(v4) dst_sel:DWORD dst_unused:UNUSED_PAD src0_sel:DWORD src1_sel:BYTE_0
	v_add_u32_sdwa v4, v1, sext(v4) dst_sel:DWORD dst_unused:UNUSED_PAD src0_sel:DWORD src1_sel:WORD_0
	v_lshlrev_b32_e32 v1, 1, v5
	v_lshrrev_b32_e32 v8, 2, v5
	v_and_b32_e32 v7, 3, v7
	s_mov_b32 s8, 0x1ffffe0
	v_and_b32_e32 v1, 24, v1
	v_and_b32_e32 v8, 4, v8
	v_and_or_b32 v7, v5, s8, v7
	v_add_u32_e32 v3, 0x2000, v3
	v_or3_b32 v1, v7, v8, v1
	v_ashrrev_i32_e32 v7, 31, v3
	v_lshrrev_b32_e32 v7, 22, v7
	v_add_u32_e32 v7, v3, v7
	v_ashrrev_i32_e32 v7, 10, v7
	v_mul_i32_i24_e32 v8, 0x400, v7
	v_sub_u32_e32 v3, v3, v8
	v_lshrrev_b32_e32 v8, 4, v3
	v_bitop3_b32 v3, v8, v3, 32 bitop3:0x6c
	v_ashrrev_i32_e32 v9, 31, v3
	s_load_dwordx2 s[0:1], s[0:1], 0x130
	v_lshrrev_b32_e32 v9, 26, v9
	v_add_u32_e32 v9, v3, v9
	v_lshlrev_b32_e32 v8, 3, v7
	v_ashrrev_i32_e32 v10, 6, v9
	v_and_b32_e32 v9, 0xc0, v9
	v_and_b32_e32 v8, -16, v8
	v_lshlrev_b32_e32 v7, 5, v7
	v_sub_u32_e32 v3, v3, v9
	v_add_u32_e32 v8, v10, v8
	v_and_b32_e32 v7, 32, v7
	v_ashrrev_i16_sdwa v3, v6, sext(v3) dst_sel:DWORD dst_unused:UNUSED_PAD src0_sel:DWORD src1_sel:BYTE_0
	s_waitcnt lgkmcnt(0)
	s_add_u32 s4, s0, 0x2d000000
	v_add_u32_sdwa v3, v7, sext(v3) dst_sel:DWORD dst_unused:UNUSED_PAD src0_sel:DWORD src1_sel:WORD_0
	v_lshlrev_b32_e32 v6, 1, v8
	v_lshrrev_b32_e32 v7, 2, v8
	v_and_b32_e32 v9, 3, v10
	s_addc_u32 s5, s1, 0
	v_and_b32_e32 v6, 24, v6
	v_and_b32_e32 v7, 4, v7
	v_and_or_b32 v9, v8, s8, v9
	s_add_u32 s6, s0, 0x1480000
	v_or3_b32 v6, v9, v7, v6
	s_addc_u32 s7, s1, 0
	v_mul_lo_u32 v1, v1, s10
	v_mul_lo_u32 v6, v6, s10
	s_ashr_i32 s10, s12, 6
	v_readlane_b32 s8, v254, 12
	s_ashr_i32 s3, s12, 8
	s_lshl_b32 s13, s10, 10
	v_readlane_b32 s9, v254, 13
	s_movk_i32 s14, 0xc1
	s_and_b64 s[8:9], s[8:9], exec
	s_cselect_b32 s8, s14, 0xc0
	v_readlane_b32 s9, v254, 9
	s_mul_i32 s8, s9, s8
	v_readlane_b32 s9, v254, 8
	s_add_i32 s8, s8, s9
	s_mul_hi_i32 s9, s8, 0x2aaaaaab
	s_lshr_b32 s11, s9, 31
	s_ashr_i32 s9, s9, 4
	s_add_i32 s9, s9, s11
	s_lshl_b32 s11, s9, 3
	s_mulk_i32 s9, 0x60
	s_sub_i32 s8, s8, s9
	s_bfe_i32 s9, s8, 0x80000
	s_bfe_u32 s9, s9, 0x3000c
	s_add_i32 s9, s8, s9
	s_bfe_i32 s15, s9, 0x80000
	s_and_b32 s9, s9, 0xf8
	s_sub_i32 s8, s8, s9
	s_sext_i32_i8 s8, s8
	s_sext_i32_i16 s15, s15
	s_add_i32 s36, s11, s8
	s_movk_i32 s8, 0x300
	s_ashr_i32 s35, s15, 3
	v_mul_lo_u32 v5, v5, s8
	v_add_lshl_u32 v1, v1, v4, 1
	v_lshl_add_u32 v135, v4, 1, v5
	v_mul_lo_u32 v4, v8, s8
	s_mul_i32 s42, s35, 0x30000
	s_cmp_gt_i32 s35, 7
	s_cselect_b32 s15, 0x100, 0
	s_add_i32 s42, s42, s15
	s_add_i32 s15, s13, 0
	v_add_lshl_u32 v134, v6, v3, 1
	v_lshl_add_u32 v136, v3, 1, v4
	s_add_i32 m0, s15, 0x10000
	v_add_u32_e32 v3, s42, v1
	global_load_lds_dwordx4 v3, s[6:7]
	v_add_u32_e32 v3, s42, v134
	s_add_i32 m0, s15, 0x12000
	s_mul_i32 s41, s36, 0x30000
	s_cmp_gt_i32 s35, 7
	s_cselect_b32 s16, 0x100, 0
	s_add_i32 s41, s41, s16
	global_load_lds_dwordx4 v3, s[6:7]
	v_add_u32_e32 v3, s41, v135
	s_mov_b32 m0, s15
	s_add_i32 s16, s15, 0x2000
	global_load_lds_dwordx4 v3, s[4:5]
	v_add_u32_e32 v3, s41, v136
	s_mov_b32 m0, s16
	s_add_i32 s8, s42, 0x18000
	global_load_lds_dwordx4 v3, s[4:5]
	s_add_i32 m0, s15, 0x14000
	v_add_u32_e32 v3, s8, v1
	v_add_u32_e32 v137, 0x18000, v135
	global_load_lds_dwordx4 v3, s[6:7]
	v_add_u32_e32 v3, s8, v134
	s_add_i32 m0, s15, 0x16000
	s_add_i32 s17, s15, 0x4000
	v_add_u32_e32 v138, 0x18000, v136
	global_load_lds_dwordx4 v3, s[6:7]
	v_add_u32_e32 v3, s41, v137
	s_mov_b32 m0, s17
	s_add_i32 s18, s15, 0x6000
	global_load_lds_dwordx4 v3, s[4:5]
	v_add_u32_e32 v3, s41, v138
	s_mov_b32 m0, s18
	s_cmp_lg_u32 s3, 1
	global_load_lds_dwordx4 v3, s[4:5]
	s_mov_b32 s19, 0
	s_cbranch_scc1 .LBB0_1147
	s_barrier
.LBB0_1147:
	s_add_u32 s8, s0, 0x1d000000
	s_addc_u32 s9, s1, 0
	s_or_b32 s0, s42, 0x80
	s_add_i32 m0, s15, 0x18000
	v_add_u32_e32 v3, s0, v1
	s_waitcnt vmcnt(4)
	s_barrier
	global_load_lds_dwordx4 v3, s[6:7]
	v_add_u32_e32 v3, s0, v134
	s_add_i32 m0, s15, 0x1a000
	s_or_b32 s0, s41, 0x80
	s_add_i32 s20, s15, 0x8000
	global_load_lds_dwordx4 v3, s[6:7]
	v_add_u32_e32 v3, s0, v135
	s_mov_b32 m0, s20
	s_add_i32 s21, s15, 0xa000
	global_load_lds_dwordx4 v3, s[4:5]
	v_add_u32_e32 v3, s0, v136
	s_mov_b32 m0, s21
	s_add_i32 s0, s42, 0x18080
	global_load_lds_dwordx4 v3, s[4:5]
	s_add_i32 m0, s15, 0x1c000
	v_add_u32_e32 v3, s0, v1
	global_load_lds_dwordx4 v3, s[6:7]
	v_add_u32_e32 v3, s0, v134
	s_add_i32 m0, s15, 0x1e000
	s_ashr_i32 s0, s2, 31
	global_load_lds_dwordx4 v3, s[6:7]
	v_bfe_u32 v139, v2, 4, 2
	s_lshr_b32 s0, s0, 26
	v_and_b32_e32 v3, 15, v2
	s_add_i32 s0, s2, s0
	v_lshlrev_b32_e32 v4, 4, v139
	v_lshlrev_b32_e32 v2, 2, v2
	s_ashr_i32 s22, s0, 6
	v_lshl_or_b32 v140, s3, 6, v3
	v_lshl_or_b32 v3, v3, 6, v4
	s_lshl_b32 s0, s3, 13
	v_and_b32_e32 v2, 32, v2
	v_bitop3_b32 v4, v3, s0, v2 bitop3:0xde
	s_lshl_b32 s0, s10, 5
	s_and_b32 s23, s0, 0x60
	s_lshl_b32 s0, s23, 7
	s_cmp_gt_i32 s2, 63
	v_bitop3_b32 v2, v3, s0, v2 bitop3:0xde
	s_waitcnt vmcnt(6)
	s_cselect_b64 s[0:1], -1, 0
	s_add_i32 s28, 0, 0x10000
	s_add_i32 s30, 0, 0x14000
	v_cndmask_b32_e64 v3, 0, 1, s[0:1]
	v_add_u32_e32 v141, s28, v2
	v_add_u32_e32 v143, s30, v2
	s_add_i32 s28, s28, s13
	s_add_i32 s30, s30, s13
	s_add_i32 s33, 0, 0x18000
	s_add_i32 s34, 0, 0x1c000
	s_cmp_gt_i32 s35, 7
	s_cselect_b32 s22, 4, 2
	s_cselect_b32 s24, 2, 0
	v_mov_b64_e32 v[130:131], 0x600
	v_mov_b64_e32 v[132:133], 0x5ff
	v_cmp_ne_u32_e64 s[0:1], 1, v3
	v_add_u32_e32 v142, 0, v4
	s_add_i32 s25, s15, 0xc000
	s_add_i32 s26, s15, 0xe000
	s_movk_i32 s27, 0x1800
	s_add_i32 s29, s28, 0x2000
	s_add_i32 s31, s30, 0x2000
	v_add_u32_e32 v144, s33, v2
	v_add_u32_e32 v145, s34, v2
	s_barrier
	s_branch .LBB0_1150

.LBB0_1149:
	v_mov_b32_e32 v146, 0
	s_lshl_b32 s10, s36, 8
	v_mov_b64_e32 v[148:149], s[8:9]
	v_add3_u32 v152, s10, v140, v146
	s_lshl_b32 s10, s35, 8
	v_add_u32_e32 v147, v146, v139
	s_or_b32 s10, s10, s23
	v_lshl_add_u32 v146, v147, 3, s10
	v_ashrrev_i32_e32 v147, 31, v146
	v_mad_i64_i32 v[150:151], s[10:11], v152, s27, v[148:149]
	v_lshlrev_b64 v[146:147], 1, v[146:147]
	v_lshl_add_u64 v[150:151], v[150:151], 0, v[146:147]
	v_cvt_pk_bf16_f32 v122, v122, v123
	v_cvt_pk_bf16_f32 v123, v124, v125
	v_cvt_pk_bf16_f32 v124, v126, v127
	v_cvt_pk_bf16_f32 v125, v128, v129
	global_store_dwordx4 v[150:151], v[122:125], off
	v_cvt_pk_bf16_f32 v118, v118, v119
	v_cvt_pk_bf16_f32 v119, v120, v121
	v_cvt_pk_bf16_f32 v120, v114, v115
	v_add_u32_e32 v114, 16, v152
	v_mad_i64_i32 v[114:115], s[10:11], v114, s27, v[148:149]
	v_lshl_add_u64 v[114:115], v[114:115], 0, v[146:147]
	v_cvt_pk_bf16_f32 v121, v116, v117
	global_store_dwordx4 v[150:151], v[118:121], off offset:256
	v_cvt_pk_bf16_f32 v110, v110, v111
	v_cvt_pk_bf16_f32 v111, v112, v113
	v_cvt_pk_bf16_f32 v112, v106, v107
	v_cvt_pk_bf16_f32 v113, v108, v109
	global_store_dwordx4 v[114:115], v[110:113], off
	v_cvt_pk_bf16_f32 v102, v102, v103
	v_cvt_pk_bf16_f32 v103, v104, v105
	v_cvt_pk_bf16_f32 v104, v98, v99
	v_add_u32_e32 v98, 32, v152
	v_mad_i64_i32 v[98:99], s[10:11], v98, s27, v[148:149]
	v_lshl_add_u64 v[98:99], v[98:99], 0, v[146:147]
	v_cvt_pk_bf16_f32 v105, v100, v101
	global_store_dwordx4 v[114:115], v[102:105], off offset:256
	v_cvt_pk_bf16_f32 v94, v94, v95
	v_cvt_pk_bf16_f32 v95, v96, v97
	v_cvt_pk_bf16_f32 v96, v90, v91
	v_cvt_pk_bf16_f32 v97, v92, v93
	global_store_dwordx4 v[98:99], v[94:97], off
	v_cvt_pk_bf16_f32 v86, v86, v87
	v_cvt_pk_bf16_f32 v87, v88, v89
	v_cvt_pk_bf16_f32 v88, v82, v83
	v_add_u32_e32 v82, 48, v152
	v_mad_i64_i32 v[82:83], s[10:11], v82, s27, v[148:149]
	v_lshl_add_u64 v[82:83], v[82:83], 0, v[146:147]
	v_cvt_pk_bf16_f32 v89, v84, v85
	global_store_dwordx4 v[98:99], v[86:89], off offset:256
	v_cvt_pk_bf16_f32 v78, v78, v79
	v_cvt_pk_bf16_f32 v79, v80, v81
	v_cvt_pk_bf16_f32 v80, v74, v75
	v_cvt_pk_bf16_f32 v81, v76, v77
	global_store_dwordx4 v[82:83], v[78:81], off
	v_cvt_pk_bf16_f32 v70, v70, v71
	v_cvt_pk_bf16_f32 v71, v72, v73
	v_cvt_pk_bf16_f32 v72, v66, v67
	v_add_u32_e32 v66, 0x80, v152
	v_mad_i64_i32 v[66:67], s[10:11], v66, s27, v[148:149]
	v_lshl_add_u64 v[66:67], v[66:67], 0, v[146:147]
	v_cvt_pk_bf16_f32 v73, v68, v69
	global_store_dwordx4 v[82:83], v[70:73], off offset:256
	v_cvt_pk_bf16_f32 v62, v62, v63
	v_cvt_pk_bf16_f32 v63, v64, v65
	v_cvt_pk_bf16_f32 v64, v58, v59
	v_cvt_pk_bf16_f32 v65, v60, v61
	global_store_dwordx4 v[66:67], v[62:65], off
	v_cvt_pk_bf16_f32 v54, v54, v55
	v_cvt_pk_bf16_f32 v55, v56, v57
	v_cvt_pk_bf16_f32 v56, v50, v51
	v_add_u32_e32 v50, 0x90, v152
	v_mad_i64_i32 v[50:51], s[10:11], v50, s27, v[148:149]
	v_lshl_add_u64 v[50:51], v[50:51], 0, v[146:147]
	v_cvt_pk_bf16_f32 v57, v52, v53
	global_store_dwordx4 v[66:67], v[54:57], off offset:256
	v_cvt_pk_bf16_f32 v46, v46, v47
	v_cvt_pk_bf16_f32 v47, v48, v49
	v_cvt_pk_bf16_f32 v48, v42, v43
	v_cvt_pk_bf16_f32 v49, v44, v45
	global_store_dwordx4 v[50:51], v[46:49], off
	v_cvt_pk_bf16_f32 v38, v38, v39
	v_cvt_pk_bf16_f32 v39, v40, v41
	v_cvt_pk_bf16_f32 v40, v34, v35
	v_add_u32_e32 v34, 0xa0, v152
	v_mad_i64_i32 v[34:35], s[10:11], v34, s27, v[148:149]
	v_lshl_add_u64 v[34:35], v[34:35], 0, v[146:147]
	v_cvt_pk_bf16_f32 v41, v36, v37
	global_store_dwordx4 v[50:51], v[38:41], off offset:256
	v_cvt_pk_bf16_f32 v30, v30, v31
	v_cvt_pk_bf16_f32 v31, v32, v33
	v_cvt_pk_bf16_f32 v32, v26, v27
	v_cvt_pk_bf16_f32 v33, v28, v29
	global_store_dwordx4 v[34:35], v[30:33], off
	v_cvt_pk_bf16_f32 v22, v22, v23
	v_cvt_pk_bf16_f32 v23, v24, v25
	v_cvt_pk_bf16_f32 v24, v18, v19
	v_add_u32_e32 v18, 0xb0, v152
	v_mad_i64_i32 v[18:19], s[10:11], v18, s27, v[148:149]
	v_lshl_add_u64 v[18:19], v[18:19], 0, v[146:147]
	s_and_b64 vcc, exec, s[2:3]
	s_mov_b32 s35, s37
	s_mov_b32 s36, s38
	s_mov_b32 s42, s40
	s_mov_b32 s41, s39
	s_cmp_gt_i32 s37, 7
	s_cselect_b32 s22, 4, 2
	s_cselect_b32 s24, 2, 0
	v_cvt_pk_bf16_f32 v25, v20, v21
	global_store_dwordx4 v[34:35], v[22:25], off offset:256
	v_cvt_pk_bf16_f32 v14, v14, v15
	v_cvt_pk_bf16_f32 v15, v16, v17
	v_cvt_pk_bf16_f32 v16, v10, v11
	v_cvt_pk_bf16_f32 v17, v12, v13
	global_store_dwordx4 v[18:19], v[14:17], off
	v_cvt_pk_bf16_f32 v6, v6, v7
	v_cvt_pk_bf16_f32 v7, v8, v9
	v_cvt_pk_bf16_f32 v8, v2, v3
	v_cvt_pk_bf16_f32 v9, v4, v5
	global_store_dwordx4 v[18:19], v[6:9], off offset:256
	s_cbranch_vccnz .LBB0_1155

.LBB0_1152:
	s_mul_i32 s39, s38, 0x30000
	s_mul_i32 s40, s37, 0x30000
	s_cmp_gt_i32 s37, 7
	s_cselect_b32 s43, 0x100, 0
	s_add_i32 s39, s39, s43
	s_add_i32 s40, s40, s43
	s_and_b64 vcc, exec, s[0:1]
	v_mov_b32_e32 v125, 0
	s_cbranch_vccnz .LBB0_1148
	v_cmp_lt_i64_e32 vcc, s[10:11], v[130:131]
	s_and_b64 s[10:11], vcc, exec
	v_mov_b32_e32 v2, 0
	s_cselect_b32 s10, s39, s41
	s_cselect_b32 s11, s40, s42
	s_addk_i32 s41, 0x80
	s_addk_i32 s42, 0x100
	s_mov_b32 s43, 0
	v_mov_b32_e32 v3, v2
	v_mov_b32_e32 v4, v2
	v_mov_b32_e32 v5, v2
	v_mov_b32_e32 v6, v2
	v_mov_b32_e32 v7, v2
	v_mov_b32_e32 v8, v2
	v_mov_b32_e32 v9, v2
	v_mov_b32_e32 v18, v2
	v_mov_b32_e32 v19, v2
	v_mov_b32_e32 v20, v2
	v_mov_b32_e32 v21, v2
	v_mov_b32_e32 v22, v2
	v_mov_b32_e32 v23, v2
	v_mov_b32_e32 v24, v2
	v_mov_b32_e32 v25, v2
	v_mov_b32_e32 v34, v2
	v_mov_b32_e32 v35, v2
	v_mov_b32_e32 v36, v2
	v_mov_b32_e32 v37, v2
	v_mov_b32_e32 v38, v2
	v_mov_b32_e32 v39, v2
	v_mov_b32_e32 v40, v2
	v_mov_b32_e32 v41, v2
	v_mov_b32_e32 v50, v2
	v_mov_b32_e32 v51, v2
	v_mov_b32_e32 v52, v2
	v_mov_b32_e32 v53, v2
	v_mov_b32_e32 v54, v2
	v_mov_b32_e32 v55, v2
	v_mov_b32_e32 v56, v2
	v_mov_b32_e32 v57, v2
	v_mov_b32_e32 v10, v2
	v_mov_b32_e32 v11, v2
	v_mov_b32_e32 v12, v2
	v_mov_b32_e32 v13, v2
	v_mov_b32_e32 v14, v2
	v_mov_b32_e32 v15, v2
	v_mov_b32_e32 v16, v2
	v_mov_b32_e32 v17, v2
	v_mov_b32_e32 v26, v2
	v_mov_b32_e32 v27, v2
	v_mov_b32_e32 v28, v2
	v_mov_b32_e32 v29, v2
	v_mov_b32_e32 v30, v2
	v_mov_b32_e32 v31, v2
	v_mov_b32_e32 v32, v2
	v_mov_b32_e32 v33, v2
	v_mov_b32_e32 v42, v2
	v_mov_b32_e32 v43, v2
	v_mov_b32_e32 v44, v2
	v_mov_b32_e32 v45, v2
	v_mov_b32_e32 v46, v2
	v_mov_b32_e32 v47, v2
	v_mov_b32_e32 v48, v2
	v_mov_b32_e32 v49, v2
	v_mov_b32_e32 v58, v2
	v_mov_b32_e32 v59, v2
	v_mov_b32_e32 v60, v2
	v_mov_b32_e32 v61, v2
	v_mov_b32_e32 v62, v2
	v_mov_b32_e32 v63, v2
	v_mov_b32_e32 v64, v2
	v_mov_b32_e32 v65, v2
	v_mov_b32_e32 v66, v2
	v_mov_b32_e32 v67, v2
	v_mov_b32_e32 v68, v2
	v_mov_b32_e32 v69, v2
	v_mov_b32_e32 v70, v2
	v_mov_b32_e32 v71, v2
	v_mov_b32_e32 v72, v2
	v_mov_b32_e32 v73, v2
	v_mov_b32_e32 v82, v2
	v_mov_b32_e32 v83, v2
	v_mov_b32_e32 v84, v2
	v_mov_b32_e32 v85, v2
	v_mov_b32_e32 v86, v2
	v_mov_b32_e32 v87, v2
	v_mov_b32_e32 v88, v2
	v_mov_b32_e32 v89, v2
	v_mov_b32_e32 v98, v2
	v_mov_b32_e32 v99, v2
	v_mov_b32_e32 v100, v2
	v_mov_b32_e32 v101, v2
	v_mov_b32_e32 v102, v2
	v_mov_b32_e32 v103, v2
	v_mov_b32_e32 v104, v2
	v_mov_b32_e32 v105, v2
	v_mov_b32_e32 v114, v2
	v_mov_b32_e32 v115, v2
	v_mov_b32_e32 v116, v2
	v_mov_b32_e32 v117, v2
	v_mov_b32_e32 v118, v2
	v_mov_b32_e32 v119, v2
	v_mov_b32_e32 v120, v2
	v_mov_b32_e32 v121, v2
	v_mov_b32_e32 v74, v2
	v_mov_b32_e32 v75, v2
	v_mov_b32_e32 v76, v2
	v_mov_b32_e32 v77, v2
	v_mov_b32_e32 v78, v2
	v_mov_b32_e32 v79, v2
	v_mov_b32_e32 v80, v2
	v_mov_b32_e32 v81, v2
	v_mov_b32_e32 v90, v2
	v_mov_b32_e32 v91, v2
	v_mov_b32_e32 v92, v2
	v_mov_b32_e32 v93, v2
	v_mov_b32_e32 v94, v2
	v_mov_b32_e32 v95, v2
	v_mov_b32_e32 v96, v2
	v_mov_b32_e32 v97, v2
	v_mov_b32_e32 v106, v2
	v_mov_b32_e32 v107, v2
	v_mov_b32_e32 v108, v2
	v_mov_b32_e32 v109, v2
	v_mov_b32_e32 v110, v2
	v_mov_b32_e32 v111, v2
	v_mov_b32_e32 v112, v2
	v_mov_b32_e32 v113, v2
	v_mov_b32_e32 v126, v2
	v_mov_b32_e32 v127, v2
	v_mov_b32_e32 v128, v2
	v_mov_b32_e32 v129, v2
	v_mov_b32_e32 v122, v2
	v_mov_b32_e32 v123, v2
	v_mov_b32_e32 v124, v2
	v_mov_b32_e32 v125, v2
